# strategy 7: DPP/permlane-swap lane permutes instead of ds_bpermute round trips in the P7 router top-k loop
# speedup vs baseline: 1.0181x; 1.0060x over previous
.LBB0_1143:
	s_mov_b32 s98, 0xffff0000
	s_mov_b32 s99, 0xffff0000
	s_mov_b32 s100, 0
	s_mov_b32 s101, -1
	s_or_b32 s74, s16, s62
	v_lshl_add_u32 v66, s74, 8, v194
	ds_read2st64_b32 v[66:67], v66 offset1:16
	s_waitcnt lgkmcnt(0)
	v_add_f32_e32 v66, v66, v67
	v_mul_f32_e32 v67, 0xbfb8aa3b, v66
	v_fma_f32 v68, v66, s70, -v67
	v_rndne_f32_e32 v69, v67
	v_fmac_f32_e32 v68, 0xb2a5705f, v66
	v_sub_f32_e32 v67, v67, v69
	v_add_f32_e32 v67, v67, v68
	v_exp_f32_e32 v67, v67
	v_cvt_i32_f32_e32 v68, v69
	v_cmp_nlt_f32_e32 vcc, s71, v66
	v_ldexp_f32 v67, v67, v68
	s_nop 0
	v_cndmask_b32_e32 v67, 0, v67, vcc
	v_cmp_ngt_f32_e32 vcc, s72, v66
	s_nop 1
	v_cndmask_b32_e32 v66, v204, v67, vcc
	v_add_f32_e32 v66, 1.0, v66
	v_div_scale_f32 v67, s[16:17], v66, v66, 1.0
	v_rcp_f32_e32 v68, v67
	s_nop 0
	v_fma_f32 v69, -v67, v68, 1.0
	v_fmac_f32_e32 v68, v69, v68
	v_div_scale_f32 v69, vcc, 1.0, v66, 1.0
	v_mul_f32_e32 v70, v69, v68
	v_fma_f32 v71, -v67, v70, v69
	v_fmac_f32_e32 v70, v71, v68
	v_fma_f32 v67, -v67, v70, v69
	v_div_fmas_f32 v67, v67, v68, v70
	v_div_fixup_f32 v66, v67, v66, 1.0
	global_load_dword v67, v[92:93], off
	s_waitcnt vmcnt(0)
	v_add_f32_e32 v67, v67, v66
	s_nop 1
	v_mov_b32_dpp v68, v67 quad_perm:[1,0,3,2] row_mask:0xf bank_mask:0xf
	s_waitcnt lgkmcnt(0)
	v_max_f32_e32 v68, v68, v68
	v_max_f32_e32 v68, v67, v68
	s_nop 1
	v_mov_b32_dpp v69, v68 quad_perm:[2,3,0,1] row_mask:0xf bank_mask:0xf
	s_waitcnt lgkmcnt(0)
	v_max_f32_e32 v69, v69, v69
	v_max_f32_e32 v68, v68, v69
	s_nop 1
	v_mov_b32_dpp v69, v68 row_shl:4 row_mask:0xf bank_mask:0x5
	v_mov_b32_dpp v69, v68 row_shr:4 row_mask:0xf bank_mask:0xa
	s_waitcnt lgkmcnt(0)
	v_max_f32_e32 v69, v69, v69
	v_max_f32_e32 v70, v68, v69
	v_cmp_eq_f32_e32 vcc, v67, v70
	s_nop 1
	v_and_b32_e32 v69, vcc_hi, v87
	v_and_b32_e32 v68, vcc_lo, v86
	v_cmp_ne_u64_e32 vcc, 0, v[68:69]
	v_ffbl_b32_e32 v69, v69
	v_add_u32_e32 v69, 32, v69
	v_ffbl_b32_e32 v68, v68
	v_min_u32_e32 v68, v68, v69
	v_cmp_eq_u32_e64 s[16:17], v206, v68
	s_and_b64 vcc, vcc, s[16:17]
	v_cndmask_b32_e32 v68, v67, v205, vcc
	s_nop 1
	v_mov_b32_dpp v69, v68 quad_perm:[1,0,3,2] row_mask:0xf bank_mask:0xf
	s_waitcnt lgkmcnt(0)
	v_max_f32_e32 v69, v69, v69
	v_max_f32_e32 v68, v68, v69
	s_nop 1
	v_mov_b32_dpp v69, v68 quad_perm:[2,3,0,1] row_mask:0xf bank_mask:0xf
	s_waitcnt lgkmcnt(0)
	v_max_f32_e32 v69, v69, v69
	v_max_f32_e32 v68, v68, v69
	s_nop 1
	v_mov_b32_dpp v69, v68 row_shl:4 row_mask:0xf bank_mask:0x5
	v_mov_b32_dpp v69, v68 row_shr:4 row_mask:0xf bank_mask:0xa
	s_waitcnt lgkmcnt(0)
	v_max_f32_e32 v69, v69, v69
	v_max_f32_e32 v68, v68, v69
	v_add_f32_e32 v68, v70, v68
	s_nop 0
	v_readlane_b32 s16, v68, 0
	s_nop 1
	v_cmp_gt_f32_e32 vcc, s16, v68
	v_cmp_eq_f32_e64 s[16:17], s16, v68
	s_and_b64 s[16:17], s[2:3], s[16:17]
	s_or_b64 s[16:17], vcc, s[16:17]
	v_cndmask_b32_e64 v69, 0, 1, s[16:17]
	v_readlane_b32 s16, v68, 8
	s_nop 1
	v_cmp_gt_f32_e32 vcc, s16, v68
	v_cmp_eq_f32_e64 s[16:17], s16, v68
	s_and_b64 s[16:17], s[4:5], s[16:17]
	s_or_b64 s[16:17], vcc, s[16:17]
	v_cndmask_b32_e64 v70, 0, 1, s[16:17]
	v_readlane_b32 s16, v68, 16
	s_nop 1
	v_cmp_gt_f32_e32 vcc, s16, v68
	v_cmp_eq_f32_e64 s[16:17], s16, v68
	s_and_b64 s[16:17], s[6:7], s[16:17]
	s_or_b64 s[16:17], vcc, s[16:17]
	v_cndmask_b32_e64 v71, 0, 1, s[16:17]
	v_readlane_b32 s16, v68, 24
	v_add3_u32 v69, v69, v70, v71
	s_nop 0
	v_cmp_gt_f32_e32 vcc, s16, v68
	v_cmp_eq_f32_e64 s[16:17], s16, v68
	s_and_b64 s[16:17], s[8:9], s[16:17]
	s_or_b64 s[16:17], vcc, s[16:17]
	v_cndmask_b32_e64 v70, 0, 1, s[16:17]
	v_readlane_b32 s16, v68, 32
	s_nop 1
	v_cmp_gt_f32_e32 vcc, s16, v68
	v_cmp_eq_f32_e64 s[16:17], s16, v68
	s_and_b64 s[16:17], s[10:11], s[16:17]
	s_or_b64 s[16:17], vcc, s[16:17]
	v_cndmask_b32_e64 v71, 0, 1, s[16:17]
	v_readlane_b32 s16, v68, 40
	v_add3_u32 v69, v69, v70, v71
	s_nop 0
	v_cmp_gt_f32_e32 vcc, s16, v68
	v_cmp_eq_f32_e64 s[16:17], s16, v68
	s_and_b64 s[16:17], s[12:13], s[16:17]
	s_or_b64 s[16:17], vcc, s[16:17]
	v_cndmask_b32_e64 v70, 0, 1, s[16:17]
	v_readlane_b32 s16, v68, 48
	s_nop 1
	v_cmp_gt_f32_e32 vcc, s16, v68
	v_cmp_eq_f32_e64 s[16:17], s16, v68
	s_and_b64 s[16:17], s[14:15], s[16:17]
	s_or_b64 s[16:17], vcc, s[16:17]
	v_cndmask_b32_e64 v71, 0, 1, s[16:17]
	v_readlane_b32 s16, v68, 56
	s_nop 1
	v_cmp_gt_f32_e32 vcc, s16, v68
	s_nop 1
	v_addc_co_u32_e32 v68, vcc, v69, v70, vcc
	v_add_u32_e32 v68, v68, v71
	v_cmp_gt_u32_e32 vcc, 4, v68
	s_nop 1
	v_cndmask_b32_e32 v67, v205, v67, vcc
	s_nop 1
	v_mov_b32_dpp v68, v67 quad_perm:[1,0,3,2] row_mask:0xf bank_mask:0xf
	s_waitcnt lgkmcnt(0)
	v_max_f32_e32 v68, v68, v68
	v_max_f32_e32 v68, v67, v68
	s_nop 1
	v_mov_b32_dpp v69, v68 quad_perm:[2,3,0,1] row_mask:0xf bank_mask:0xf
	s_waitcnt lgkmcnt(0)
	v_max_f32_e32 v69, v69, v69
	v_max_f32_e32 v68, v68, v69
	s_nop 1
	v_mov_b32_dpp v69, v68 row_shl:4 row_mask:0xf bank_mask:0x5
	v_mov_b32_dpp v69, v68 row_shr:4 row_mask:0xf bank_mask:0xa
	s_waitcnt lgkmcnt(0)
	v_max_f32_e32 v69, v69, v69
	v_max_f32_e32 v68, v68, v69
	s_nop 1
	v_mov_b32_dpp v69, v68 row_ror:8 row_mask:0xf bank_mask:0xf
	s_waitcnt lgkmcnt(0)
	v_max_f32_e32 v69, v69, v69
	v_max_f32_e32 v68, v68, v69
	v_mov_b32_e32 v69, v68
	v_mov_b32_e32 v239, v68
	s_nop 1
	v_permlane16_swap_b32_e32 v69, v239
	v_cndmask_b32_e64 v69, v239, v69, s[98:99]
	s_waitcnt lgkmcnt(0)
	v_max_f32_e32 v69, v69, v69
	v_max_f32_e32 v68, v68, v69
	v_mov_b32_e32 v69, v68
	v_mov_b32_e32 v239, v68
	s_nop 1
	v_permlane32_swap_b32_e32 v69, v239
	v_cndmask_b32_e64 v69, v239, v69, s[100:101]
	s_waitcnt lgkmcnt(0)
	v_max_f32_e32 v69, v69, v69
	v_max_f32_e32 v68, v68, v69
	v_cmp_eq_f32_e32 vcc, v67, v68
	s_cmp_lg_u64 vcc, 0
	s_ff1_i32_b64 s18, vcc
	s_cselect_b64 s[16:17], -1, 0
	v_cmp_eq_u32_e32 vcc, s18, v206
	s_and_b64 vcc, s[16:17], vcc
	s_nop 0
	v_cndmask_b32_e32 v67, v67, v205, vcc
	s_nop 1
	v_mov_b32_dpp v68, v67 quad_perm:[1,0,3,2] row_mask:0xf bank_mask:0xf
	s_waitcnt lgkmcnt(0)
	v_max_f32_e32 v68, v68, v68
	v_max_f32_e32 v68, v67, v68
	s_nop 1
	v_mov_b32_dpp v69, v68 quad_perm:[2,3,0,1] row_mask:0xf bank_mask:0xf
	s_waitcnt lgkmcnt(0)
	v_max_f32_e32 v69, v69, v69
	v_max_f32_e32 v68, v68, v69
	s_nop 1
	v_mov_b32_dpp v69, v68 row_shl:4 row_mask:0xf bank_mask:0x5
	v_mov_b32_dpp v69, v68 row_shr:4 row_mask:0xf bank_mask:0xa
	s_waitcnt lgkmcnt(0)
	v_max_f32_e32 v69, v69, v69
	v_max_f32_e32 v68, v68, v69
	s_nop 1
	v_mov_b32_dpp v69, v68 row_ror:8 row_mask:0xf bank_mask:0xf
	s_waitcnt lgkmcnt(0)
	v_max_f32_e32 v69, v69, v69
	v_max_f32_e32 v68, v68, v69
	v_mov_b32_e32 v69, v68
	v_mov_b32_e32 v239, v68
	s_nop 1
	v_permlane16_swap_b32_e32 v69, v239
	v_cndmask_b32_e64 v69, v239, v69, s[98:99]
	s_waitcnt lgkmcnt(0)
	v_max_f32_e32 v69, v69, v69
	v_max_f32_e32 v68, v68, v69
	v_mov_b32_e32 v69, v68
	v_mov_b32_e32 v239, v68
	s_nop 1
	v_permlane32_swap_b32_e32 v69, v239
	v_cndmask_b32_e64 v69, v239, v69, s[100:101]
	s_waitcnt lgkmcnt(0)
	v_max_f32_e32 v69, v69, v69
	v_max_f32_e32 v68, v68, v69
	v_cmp_eq_f32_e64 s[16:17], v67, v68
	s_cmp_lg_u64 s[16:17], 0
	s_ff1_i32_b64 s16, s[16:17]
	s_cselect_b64 s[18:19], -1, 0
	v_cmp_eq_u32_e64 s[16:17], s16, v206
	s_and_b64 s[16:17], s[18:19], s[16:17]
	s_nop 0
	v_cndmask_b32_e64 v67, v67, v205, s[16:17]
	s_nop 1
	v_mov_b32_dpp v68, v67 quad_perm:[1,0,3,2] row_mask:0xf bank_mask:0xf
	s_waitcnt lgkmcnt(0)
	v_max_f32_e32 v68, v68, v68
	v_max_f32_e32 v68, v67, v68
	s_nop 1
	v_mov_b32_dpp v69, v68 quad_perm:[2,3,0,1] row_mask:0xf bank_mask:0xf
	s_waitcnt lgkmcnt(0)
	v_max_f32_e32 v69, v69, v69
	v_max_f32_e32 v68, v68, v69
	s_nop 1
	v_mov_b32_dpp v69, v68 row_shl:4 row_mask:0xf bank_mask:0x5
	v_mov_b32_dpp v69, v68 row_shr:4 row_mask:0xf bank_mask:0xa
	s_waitcnt lgkmcnt(0)
	v_max_f32_e32 v69, v69, v69
	v_max_f32_e32 v68, v68, v69
	s_nop 1
	v_mov_b32_dpp v69, v68 row_ror:8 row_mask:0xf bank_mask:0xf
	s_waitcnt lgkmcnt(0)
	v_max_f32_e32 v69, v69, v69
	v_max_f32_e32 v68, v68, v69
	v_mov_b32_e32 v69, v68
	v_mov_b32_e32 v239, v68
	s_nop 1
	v_permlane16_swap_b32_e32 v69, v239
	v_cndmask_b32_e64 v69, v239, v69, s[98:99]
	s_waitcnt lgkmcnt(0)
	v_max_f32_e32 v69, v69, v69
	v_max_f32_e32 v68, v68, v69
	v_mov_b32_e32 v69, v68
	v_mov_b32_e32 v239, v68
	s_nop 1
	v_permlane32_swap_b32_e32 v69, v239
	v_cndmask_b32_e64 v69, v239, v69, s[100:101]
	s_waitcnt lgkmcnt(0)
	v_max_f32_e32 v69, v69, v69
	v_max_f32_e32 v68, v68, v69
	v_cmp_eq_f32_e64 s[18:19], v67, v68
	s_cmp_lg_u64 s[18:19], 0
	s_ff1_i32_b64 s18, s[18:19]
	s_cselect_b64 s[20:21], -1, 0
	v_cmp_eq_u32_e64 s[18:19], s18, v206
	s_and_b64 s[18:19], s[20:21], s[18:19]
	s_nop 0
	v_cndmask_b32_e64 v67, v67, v205, s[18:19]
	s_nop 1
	v_mov_b32_dpp v68, v67 quad_perm:[1,0,3,2] row_mask:0xf bank_mask:0xf
	s_waitcnt lgkmcnt(0)
	v_max_f32_e32 v68, v68, v68
	v_max_f32_e32 v68, v67, v68
	s_nop 1
	v_mov_b32_dpp v69, v68 quad_perm:[2,3,0,1] row_mask:0xf bank_mask:0xf
	s_waitcnt lgkmcnt(0)
	v_max_f32_e32 v69, v69, v69
	v_max_f32_e32 v68, v68, v69
	s_nop 1
	v_mov_b32_dpp v69, v68 row_shl:4 row_mask:0xf bank_mask:0x5
	v_mov_b32_dpp v69, v68 row_shr:4 row_mask:0xf bank_mask:0xa
	s_waitcnt lgkmcnt(0)
	v_max_f32_e32 v69, v69, v69
	v_max_f32_e32 v68, v68, v69
	s_nop 1
	v_mov_b32_dpp v69, v68 row_ror:8 row_mask:0xf bank_mask:0xf
	s_waitcnt lgkmcnt(0)
	v_max_f32_e32 v69, v69, v69
	v_max_f32_e32 v68, v68, v69
	v_mov_b32_e32 v69, v68
	v_mov_b32_e32 v239, v68
	s_nop 1
	v_permlane16_swap_b32_e32 v69, v239
	v_cndmask_b32_e64 v69, v239, v69, s[98:99]
	s_waitcnt lgkmcnt(0)
	v_max_f32_e32 v69, v69, v69
	v_max_f32_e32 v68, v68, v69
	v_mov_b32_e32 v69, v68
	v_mov_b32_e32 v239, v68
	s_nop 1
	v_permlane32_swap_b32_e32 v69, v239
	v_cndmask_b32_e64 v69, v239, v69, s[100:101]
	s_waitcnt lgkmcnt(0)
	v_max_f32_e32 v69, v69, v69
	v_max_f32_e32 v68, v68, v69
	v_cmp_eq_f32_e64 s[20:21], v67, v68
	s_cmp_lg_u64 s[20:21], 0
	s_ff1_i32_b64 s20, s[20:21]
	s_cselect_b64 s[22:23], -1, 0
	v_cmp_eq_u32_e64 s[20:21], s20, v206
	s_and_b64 s[20:21], s[22:23], s[20:21]
	s_nop 0
	v_cndmask_b32_e64 v67, v67, v205, s[20:21]
	s_nop 1
	v_mov_b32_dpp v68, v67 quad_perm:[1,0,3,2] row_mask:0xf bank_mask:0xf
	s_waitcnt lgkmcnt(0)
	v_max_f32_e32 v68, v68, v68
	v_max_f32_e32 v68, v67, v68
	s_nop 1
	v_mov_b32_dpp v69, v68 quad_perm:[2,3,0,1] row_mask:0xf bank_mask:0xf
	s_waitcnt lgkmcnt(0)
	v_max_f32_e32 v69, v69, v69
	v_max_f32_e32 v68, v68, v69
	s_nop 1
	v_mov_b32_dpp v69, v68 row_shl:4 row_mask:0xf bank_mask:0x5
	v_mov_b32_dpp v69, v68 row_shr:4 row_mask:0xf bank_mask:0xa
	s_waitcnt lgkmcnt(0)
	v_max_f32_e32 v69, v69, v69
	v_max_f32_e32 v68, v68, v69
	s_nop 1
	v_mov_b32_dpp v69, v68 row_ror:8 row_mask:0xf bank_mask:0xf
	s_waitcnt lgkmcnt(0)
	v_max_f32_e32 v69, v69, v69
	v_max_f32_e32 v68, v68, v69
	v_mov_b32_e32 v69, v68
	v_mov_b32_e32 v239, v68
	s_nop 1
	v_permlane16_swap_b32_e32 v69, v239
	v_cndmask_b32_e64 v69, v239, v69, s[98:99]
	s_waitcnt lgkmcnt(0)
	v_max_f32_e32 v69, v69, v69
	v_max_f32_e32 v68, v68, v69
	v_mov_b32_e32 v69, v68
	v_mov_b32_e32 v239, v68
	s_nop 1
	v_permlane32_swap_b32_e32 v69, v239
	v_cndmask_b32_e64 v69, v239, v69, s[100:101]
	s_waitcnt lgkmcnt(0)
	v_max_f32_e32 v69, v69, v69
	v_max_f32_e32 v68, v68, v69
	v_cmp_eq_f32_e64 s[22:23], v67, v68
	s_cmp_lg_u64 s[22:23], 0
	s_ff1_i32_b64 s22, s[22:23]
	s_cselect_b64 s[24:25], -1, 0
	v_cmp_eq_u32_e64 s[22:23], s22, v206
	s_and_b64 s[22:23], s[24:25], s[22:23]
	s_nop 0
	v_cndmask_b32_e64 v67, v67, v205, s[22:23]
	s_nop 1
	v_mov_b32_dpp v68, v67 quad_perm:[1,0,3,2] row_mask:0xf bank_mask:0xf
	v_max_f32_e32 v69, v67, v67
	s_waitcnt lgkmcnt(0)
	v_max_f32_e32 v68, v68, v68
	v_max_f32_e32 v68, v69, v68
	s_nop 1
	v_mov_b32_dpp v69, v68 quad_perm:[2,3,0,1] row_mask:0xf bank_mask:0xf
	s_waitcnt lgkmcnt(0)
	v_max_f32_e32 v69, v69, v69
	v_max_f32_e32 v68, v68, v69
	s_nop 1
	v_mov_b32_dpp v69, v68 row_shl:4 row_mask:0xf bank_mask:0x5
	v_mov_b32_dpp v69, v68 row_shr:4 row_mask:0xf bank_mask:0xa
	s_waitcnt lgkmcnt(0)
	v_max_f32_e32 v69, v69, v69
	v_max_f32_e32 v68, v68, v69
	s_nop 1
	v_mov_b32_dpp v69, v68 row_ror:8 row_mask:0xf bank_mask:0xf
	s_waitcnt lgkmcnt(0)
	v_max_f32_e32 v69, v69, v69
	v_max_f32_e32 v68, v68, v69
	v_mov_b32_e32 v69, v68
	v_mov_b32_e32 v239, v68
	s_nop 1
	v_permlane16_swap_b32_e32 v69, v239
	v_cndmask_b32_e64 v69, v239, v69, s[98:99]
	s_waitcnt lgkmcnt(0)
	v_max_f32_e32 v69, v69, v69
	v_max_f32_e32 v68, v68, v69
	v_mov_b32_e32 v69, v68
	v_mov_b32_e32 v239, v68
	s_nop 1
	v_permlane32_swap_b32_e32 v69, v239
	v_cndmask_b32_e64 v69, v239, v69, s[100:101]
	s_waitcnt lgkmcnt(0)
	v_max_f32_e32 v69, v69, v69
	v_max_f32_e32 v68, v68, v69
	v_cmp_eq_f32_e64 s[24:25], v67, v68
	s_cmp_lg_u64 s[24:25], 0
	s_ff1_i32_b64 s24, s[24:25]
	s_cselect_b64 s[26:27], -1, 0
	v_cmp_eq_u32_e64 s[24:25], s24, v206
	s_and_b64 s[24:25], s[26:27], s[24:25]
	s_nop 0
	v_cndmask_b32_e64 v67, v67, v205, s[24:25]
	s_nop 1
	v_mov_b32_dpp v68, v67 quad_perm:[1,0,3,2] row_mask:0xf bank_mask:0xf
	v_max_f32_e32 v69, v67, v67
	s_waitcnt lgkmcnt(0)
	v_max_f32_e32 v68, v68, v68
	v_max_f32_e32 v68, v69, v68
	s_nop 1
	v_mov_b32_dpp v69, v68 quad_perm:[2,3,0,1] row_mask:0xf bank_mask:0xf
	s_waitcnt lgkmcnt(0)
	v_max_f32_e32 v69, v69, v69
	v_max_f32_e32 v68, v68, v69
	s_nop 1
	v_mov_b32_dpp v69, v68 row_shl:4 row_mask:0xf bank_mask:0x5
	v_mov_b32_dpp v69, v68 row_shr:4 row_mask:0xf bank_mask:0xa
	s_waitcnt lgkmcnt(0)
	v_max_f32_e32 v69, v69, v69
	v_max_f32_e32 v68, v68, v69
	s_nop 1
	v_mov_b32_dpp v69, v68 row_ror:8 row_mask:0xf bank_mask:0xf
	s_waitcnt lgkmcnt(0)
	v_max_f32_e32 v69, v69, v69
	v_max_f32_e32 v68, v68, v69
	v_mov_b32_e32 v69, v68
	v_mov_b32_e32 v239, v68
	s_nop 1
	v_permlane16_swap_b32_e32 v69, v239
	v_cndmask_b32_e64 v69, v239, v69, s[98:99]
	s_waitcnt lgkmcnt(0)
	v_max_f32_e32 v69, v69, v69
	v_max_f32_e32 v68, v68, v69
	v_mov_b32_e32 v69, v68
	v_mov_b32_e32 v239, v68
	s_nop 1
	v_permlane32_swap_b32_e32 v69, v239
	v_cndmask_b32_e64 v69, v239, v69, s[100:101]
	s_waitcnt lgkmcnt(0)
	v_max_f32_e32 v69, v69, v69
	v_max_f32_e32 v68, v68, v69
	v_cmp_eq_f32_e64 s[26:27], v67, v68
	s_cmp_lg_u64 s[26:27], 0
	s_ff1_i32_b64 s26, s[26:27]
	s_cselect_b64 s[28:29], -1, 0
	v_cmp_eq_u32_e64 s[26:27], s26, v206
	s_and_b64 s[26:27], s[28:29], s[26:27]
	s_nop 0
	v_cndmask_b32_e64 v67, v67, v205, s[26:27]
	s_nop 1
	v_mov_b32_dpp v68, v67 quad_perm:[1,0,3,2] row_mask:0xf bank_mask:0xf
	v_max_f32_e32 v69, v67, v67
	s_waitcnt lgkmcnt(0)
	v_max_f32_e32 v68, v68, v68
	v_max_f32_e32 v68, v69, v68
	s_nop 1
	v_mov_b32_dpp v69, v68 quad_perm:[2,3,0,1] row_mask:0xf bank_mask:0xf
	s_waitcnt lgkmcnt(0)
	v_max_f32_e32 v69, v69, v69
	v_max_f32_e32 v68, v68, v69
	s_nop 1
	v_mov_b32_dpp v69, v68 row_shl:4 row_mask:0xf bank_mask:0x5
	v_mov_b32_dpp v69, v68 row_shr:4 row_mask:0xf bank_mask:0xa
	s_waitcnt lgkmcnt(0)
	v_max_f32_e32 v69, v69, v69
	v_max_f32_e32 v68, v68, v69
	s_nop 1
	v_mov_b32_dpp v69, v68 row_ror:8 row_mask:0xf bank_mask:0xf
	s_waitcnt lgkmcnt(0)
	v_max_f32_e32 v69, v69, v69
	v_max_f32_e32 v68, v68, v69
	v_mov_b32_e32 v69, v68
	v_mov_b32_e32 v239, v68
	s_nop 1
	v_permlane16_swap_b32_e32 v69, v239
	v_cndmask_b32_e64 v69, v239, v69, s[98:99]
	s_waitcnt lgkmcnt(0)
	v_max_f32_e32 v69, v69, v69
	v_max_f32_e32 v68, v68, v69
	v_mov_b32_e32 v69, v68
	v_mov_b32_e32 v239, v68
	s_nop 1
	v_permlane32_swap_b32_e32 v69, v239
	v_cndmask_b32_e64 v69, v239, v69, s[100:101]
	s_waitcnt lgkmcnt(0)
	v_max_f32_e32 v69, v69, v69
	v_max_f32_e32 v68, v68, v69
	v_cmp_eq_f32_e64 s[28:29], v67, v68
	s_cmp_lg_u64 s[28:29], 0
	s_ff1_i32_b64 s28, s[28:29]
	s_cselect_b64 s[76:77], -1, 0
	v_cmp_eq_u32_e64 s[28:29], s28, v206
	s_and_b64 s[28:29], s[76:77], s[28:29]
	s_or_b64 s[26:27], s[28:29], s[26:27]
	s_or_b64 s[24:25], s[26:27], s[24:25]
	s_or_b64 s[22:23], s[24:25], s[22:23]
	s_or_b64 s[20:21], s[22:23], s[20:21]
	s_or_b64 s[18:19], s[20:21], s[18:19]
	s_or_b64 s[16:17], s[18:19], s[16:17]
	s_or_b64 s[16:17], s[16:17], vcc
	v_cndmask_b32_e64 v67, 0, v66, s[16:17]
	s_nop 1
	v_mov_b32_dpp v68, v67 quad_perm:[1,0,3,2] row_mask:0xf bank_mask:0xf
	v_cndmask_b32_e64 v69, 0, 1, s[16:17]
	v_cmp_ne_u32_e32 vcc, 0, v69
	s_waitcnt lgkmcnt(0)
	v_add_f32_e32 v67, v67, v68
	s_nop 1
	v_mov_b32_dpp v68, v67 quad_perm:[2,3,0,1] row_mask:0xf bank_mask:0xf
	s_waitcnt lgkmcnt(0)
	v_add_f32_e32 v67, v67, v68
	s_nop 1
	v_mov_b32_dpp v68, v67 row_shl:4 row_mask:0xf bank_mask:0x5
	v_mov_b32_dpp v68, v67 row_shr:4 row_mask:0xf bank_mask:0xa
	s_waitcnt lgkmcnt(0)
	v_add_f32_e32 v67, v67, v68
	s_nop 1
	v_mov_b32_dpp v68, v67 row_ror:8 row_mask:0xf bank_mask:0xf
	s_waitcnt lgkmcnt(0)
	v_add_f32_e32 v67, v67, v68
	v_mov_b32_e32 v68, v67
	v_mov_b32_e32 v239, v67
	s_nop 1
	v_permlane16_swap_b32_e32 v68, v239
	v_cndmask_b32_e64 v68, v239, v68, s[98:99]
	s_waitcnt lgkmcnt(0)
	v_add_f32_e32 v67, v67, v68
	v_mov_b32_e32 v68, v67
	v_mov_b32_e32 v239, v67
	s_nop 1
	v_permlane32_swap_b32_e32 v68, v239
	v_cndmask_b32_e64 v68, v239, v68, s[100:101]
	s_and_saveexec_b64 s[18:19], s[16:17]
	s_cbranch_execz .LBB0_1142
	s_add_i32 s74, s74, s63
	s_cmpk_gt_i32 s74, 0x3fff
	s_waitcnt lgkmcnt(0)
	v_add_f32_e32 v67, v67, v68
	v_mbcnt_lo_u32_b32 v68, vcc_lo, 0
	s_cselect_b32 s16, 0x100, 0
	v_mbcnt_hi_u32_b32 v68, vcc_hi, v68
	v_add_u32_e32 v69, s16, v115
	ds_add_rtn_u32 v72, v69, v201
	v_lshl_add_u32 v68, s74, 3, v68
	v_div_scale_f32 v73, s[16:17], v67, v67, v66
	v_ashrrev_i32_e32 v69, 31, v68
	v_rcp_f32_e32 v116, v73
	v_lshlrev_b64 v[68:69], 2, v[68:69]
	v_lshl_add_u64 v[70:71], s[36:37], 0, v[68:69]
	global_store_dword v[70:71], v206, off
	v_lshl_add_u64 v[70:71], s[38:39], 0, v[68:69]
	s_waitcnt lgkmcnt(0)
	global_store_dword v[70:71], v72, off
	v_fma_f32 v70, -v73, v116, 1.0
	v_fmac_f32_e32 v116, v70, v116
	v_div_scale_f32 v70, vcc, v66, v67, v66
	v_mul_f32_e32 v71, v70, v116
	v_fma_f32 v72, -v73, v71, v70
	v_fmac_f32_e32 v71, v72, v116
	v_fma_f32 v70, -v73, v71, v70
	v_div_fmas_f32 v70, v70, v116, v71
	v_div_fixup_f32 v66, v70, v67, v66
	v_mul_f32_e32 v70, 0x40200000, v66
	v_lshl_add_u64 v[66:67], s[40:41], 0, v[68:69]
	global_store_dword v[66:67], v70, off
	s_branch .LBB0_1142
